# attention unit loops: the next-unit dequeue atomic is no longer waited right after issue; it returns into the index register and is covered by the unit's later in-order waits, on top of v062
# speedup vs baseline: 1.0029x; 1.0001x over previous
.LBB0_354:
	v_mov_b32_e32 v198, 0
	s_and_saveexec_b64 s[8:9], s[0:1]
	s_cbranch_execz .LBB0_358
	s_mov_b64 s[12:13], exec
	v_mbcnt_lo_u32_b32 v2, s12, 0
	v_mbcnt_hi_u32_b32 v2, s13, v2
	v_cmp_eq_u32_e32 vcc, 0, v2
	s_and_saveexec_b64 s[10:11], vcc
	s_cbranch_execz .LBB0_357
	s_bcnt1_i32_b64 s12, s[12:13]
	v_mov_b32_e32 v3, s12
	global_atomic_add v198, v179, v3, s[6:7] sc0
.LBB0_357:
	s_or_b64 exec, exec, s[10:11]
.LBB0_358:
	s_or_b64 exec, exec, s[8:9]
	s_cmpk_gt_i32 s35, 0x3ff
	s_mov_b64 s[8:9], -1
	s_cbranch_scc0 .LBB0_361
	s_add_i32 s8, s35, 0xfffffc00
	s_lshr_b32 s34, s8, 3
	s_lshl_b32 s8, s34, 8
	s_add_i32 s30, s8, 0x8000
	s_mov_b32 s31, 4
	s_cbranch_execz .LBB0_362

.LBB0_380:
	s_nop 15
	s_nop 2
	v_div_scale_f32 v35, s[8:9], v34, v34, 1.0
	v_rcp_f32_e32 v36, v35
	v_readlane_b32 s8, v254, 36
	s_add_u32 s8, s8, s33
	v_readlane_b32 s9, v254, 37
	v_fma_f32 v37, -v35, v36, 1.0
	v_fmac_f32_e32 v36, v37, v36
	v_div_scale_f32 v37, vcc, 1.0, v34, 1.0
	v_mul_f32_e32 v38, v37, v36
	v_fma_f32 v39, -v35, v38, v37
	v_fmac_f32_e32 v38, v39, v36
	v_fma_f32 v35, -v35, v38, v37
	v_div_fmas_f32 v35, v35, v36, v38
	s_addc_u32 s9, s9, 0
	v_div_fixup_f32 v36, v35, v34, 1.0
	v_lshlrev_b64 v[34:35], 11, v[184:185]
	v_lshl_add_u64 v[34:35], s[8:9], 0, v[34:35]
	v_mul_f32_e32 v40, 0x41800000, v36
	v_lshl_add_u64 v[38:39], v[34:35], 0, v[182:183]
	v_mul_f32_e32 v34, v66, v40
	v_mul_f32_e32 v35, v67, v40
	v_med3_f32 v37, v34, s28, v197
	v_med3_f32 v35, v35, s28, v197
	v_mov_b32_e32 v34, 0
	v_cvt_pk_fp8_f32 v34, v37, v35
	v_mul_f32_e32 v36, v68, v40
	v_mul_f32_e32 v35, v69, v40
	v_med3_f32 v36, v36, s28, v197
	v_med3_f32 v35, v35, s28, v197
	v_cvt_pk_fp8_f32 v34, v36, v35 op_sel:[0,0,1]
	v_mul_f32_e32 v35, v70, v40
	v_mul_f32_e32 v36, v71, v40
	v_med3_f32 v35, v35, s28, v197
	v_med3_f32 v41, v36, s28, v197
	v_mov_b32_e32 v36, 0
	v_cvt_pk_fp8_f32 v36, v35, v41
	v_mul_f32_e32 v37, v72, v40
	v_mul_f32_e32 v35, v73, v40
	v_med3_f32 v37, v37, s28, v197
	v_med3_f32 v35, v35, s28, v197
	v_cvt_pk_fp8_f32 v36, v37, v35 op_sel:[0,0,1]
	v_mul_f32_e32 v35, v74, v40
	v_mul_f32_e32 v37, v75, v40
	v_med3_f32 v42, v35, s28, v197
	v_med3_f32 v37, v37, s28, v197
	v_mov_b32_e32 v35, 0
	v_cvt_pk_fp8_f32 v35, v42, v37
	v_mul_f32_e32 v41, v76, v40
	v_mul_f32_e32 v37, v77, v40
	v_med3_f32 v41, v41, s28, v197
	v_med3_f32 v37, v37, s28, v197
	v_cvt_pk_fp8_f32 v35, v41, v37 op_sel:[0,0,1]
	v_mul_f32_e32 v37, v78, v40
	v_mul_f32_e32 v41, v79, v40
	v_med3_f32 v43, v37, s28, v197
	v_med3_f32 v41, v41, s28, v197
	v_mov_b32_e32 v37, 0
	v_cvt_pk_fp8_f32 v37, v43, v41
	v_mul_f32_e32 v42, v80, v40
	v_mul_f32_e32 v41, v81, v40
	v_med3_f32 v42, v42, s28, v197
	v_med3_f32 v41, v41, s28, v197
	v_cvt_pk_fp8_f32 v37, v42, v41 op_sel:[0,0,1]
	v_permlane32_swap_b32_e32 v34, v35
	v_mul_f32_e32 v18, v18, v40
	v_permlane32_swap_b32_e32 v36, v37
	global_store_dwordx4 v[38:39], v[34:37], off
	v_mul_f32_e32 v19, v19, v40
	v_med3_f32 v19, v19, s28, v197
	v_mul_f32_e32 v34, v50, v40
	v_mul_f32_e32 v35, v51, v40
	v_med3_f32 v37, v34, s28, v197
	v_med3_f32 v35, v35, s28, v197
	v_mov_b32_e32 v34, 0
	v_cvt_pk_fp8_f32 v34, v37, v35
	v_mul_f32_e32 v36, v52, v40
	v_mul_f32_e32 v35, v53, v40
	v_med3_f32 v36, v36, s28, v197
	v_med3_f32 v35, v35, s28, v197
	v_cvt_pk_fp8_f32 v34, v36, v35 op_sel:[0,0,1]
	v_mul_f32_e32 v35, v54, v40
	v_mul_f32_e32 v36, v55, v40
	v_med3_f32 v35, v35, s28, v197
	v_med3_f32 v41, v36, s28, v197
	v_mov_b32_e32 v36, 0
	v_cvt_pk_fp8_f32 v36, v35, v41
	v_mul_f32_e32 v37, v56, v40
	v_mul_f32_e32 v35, v57, v40
	v_med3_f32 v37, v37, s28, v197
	v_med3_f32 v35, v35, s28, v197
	v_cvt_pk_fp8_f32 v36, v37, v35 op_sel:[0,0,1]
	v_mul_f32_e32 v35, v58, v40
	v_mul_f32_e32 v37, v59, v40
	v_med3_f32 v42, v35, s28, v197
	v_med3_f32 v37, v37, s28, v197
	v_mov_b32_e32 v35, 0
	v_cvt_pk_fp8_f32 v35, v42, v37
	v_mul_f32_e32 v41, v60, v40
	v_mul_f32_e32 v37, v61, v40
	v_med3_f32 v41, v41, s28, v197
	v_med3_f32 v37, v37, s28, v197
	v_cvt_pk_fp8_f32 v35, v41, v37 op_sel:[0,0,1]
	v_mul_f32_e32 v37, v62, v40
	v_mul_f32_e32 v41, v63, v40
	v_med3_f32 v43, v37, s28, v197
	v_med3_f32 v41, v41, s28, v197
	v_mov_b32_e32 v37, 0
	v_cvt_pk_fp8_f32 v37, v43, v41
	v_mul_f32_e32 v42, v64, v40
	v_mul_f32_e32 v41, v65, v40
	v_med3_f32 v42, v42, s28, v197
	v_med3_f32 v41, v41, s28, v197
	v_cvt_pk_fp8_f32 v37, v42, v41 op_sel:[0,0,1]
	v_permlane32_swap_b32_e32 v34, v35
	v_mul_f32_e32 v20, v20, v40
	v_permlane32_swap_b32_e32 v36, v37
	global_store_dwordx4 v[38:39], v[34:37], off offset:32
	v_med3_f32 v20, v20, s28, v197
	v_mul_f32_e32 v2, v2, v40
	v_med3_f32 v34, v18, s28, v197
	v_mov_b32_e32 v18, 0
	v_cvt_pk_fp8_f32 v18, v34, v19
	v_mul_f32_e32 v19, v21, v40
	v_med3_f32 v19, v19, s28, v197
	v_mul_f32_e32 v21, v24, v40
	v_cvt_pk_fp8_f32 v18, v20, v19 op_sel:[0,0,1]
	v_mul_f32_e32 v19, v22, v40
	v_mul_f32_e32 v20, v23, v40
	v_med3_f32 v19, v19, s28, v197
	v_med3_f32 v22, v20, s28, v197
	v_mov_b32_e32 v20, 0
	v_cvt_pk_fp8_f32 v20, v19, v22
	v_mul_f32_e32 v19, v25, v40
	v_med3_f32 v21, v21, s28, v197
	v_med3_f32 v19, v19, s28, v197
	v_cvt_pk_fp8_f32 v20, v21, v19 op_sel:[0,0,1]
	v_mul_f32_e32 v19, v26, v40
	v_mul_f32_e32 v21, v27, v40
	v_med3_f32 v23, v19, s28, v197
	v_med3_f32 v21, v21, s28, v197
	v_mov_b32_e32 v19, 0
	v_cvt_pk_fp8_f32 v19, v23, v21
	v_mul_f32_e32 v22, v28, v40
	v_mul_f32_e32 v21, v29, v40
	v_med3_f32 v22, v22, s28, v197
	v_med3_f32 v21, v21, s28, v197
	v_cvt_pk_fp8_f32 v19, v22, v21 op_sel:[0,0,1]
	v_mul_f32_e32 v21, v30, v40
	v_mul_f32_e32 v22, v31, v40
	v_med3_f32 v24, v21, s28, v197
	v_med3_f32 v22, v22, s28, v197
	v_mov_b32_e32 v21, 0
	v_cvt_pk_fp8_f32 v21, v24, v22
	v_mul_f32_e32 v23, v32, v40
	v_mul_f32_e32 v22, v33, v40
	v_med3_f32 v23, v23, s28, v197
	v_med3_f32 v22, v22, s28, v197
	v_cvt_pk_fp8_f32 v21, v23, v22 op_sel:[0,0,1]
	v_permlane32_swap_b32_e32 v18, v19
	v_mul_f32_e32 v3, v3, v40
	v_permlane32_swap_b32_e32 v20, v21
	global_store_dwordx4 v[38:39], v[18:21], off offset:64
	v_med3_f32 v3, v3, s28, v197
	v_mul_f32_e32 v4, v4, v40
	v_med3_f32 v18, v2, s28, v197
	v_mov_b32_e32 v2, 0
	v_cvt_pk_fp8_f32 v2, v18, v3
	v_mul_f32_e32 v3, v5, v40
	v_med3_f32 v4, v4, s28, v197
	v_med3_f32 v3, v3, s28, v197
	v_cvt_pk_fp8_f32 v2, v4, v3 op_sel:[0,0,1]
	v_mul_f32_e32 v3, v6, v40
	v_mul_f32_e32 v4, v7, v40
	v_med3_f32 v3, v3, s28, v197
	v_med3_f32 v6, v4, s28, v197
	v_mov_b32_e32 v4, 0
	v_cvt_pk_fp8_f32 v4, v3, v6
	v_mul_f32_e32 v5, v8, v40
	v_mul_f32_e32 v3, v9, v40
	v_med3_f32 v5, v5, s28, v197
	v_med3_f32 v3, v3, s28, v197
	v_cvt_pk_fp8_f32 v4, v5, v3 op_sel:[0,0,1]
	v_mul_f32_e32 v3, v10, v40
	v_mul_f32_e32 v5, v11, v40
	v_med3_f32 v7, v3, s28, v197
	v_med3_f32 v5, v5, s28, v197
	v_mov_b32_e32 v3, 0
	v_cvt_pk_fp8_f32 v3, v7, v5
	v_mul_f32_e32 v6, v12, v40
	v_mul_f32_e32 v5, v13, v40
	v_med3_f32 v6, v6, s28, v197
	v_med3_f32 v5, v5, s28, v197
	v_cvt_pk_fp8_f32 v3, v6, v5 op_sel:[0,0,1]
	v_mul_f32_e32 v5, v14, v40
	v_mul_f32_e32 v6, v15, v40
	v_med3_f32 v8, v5, s28, v197
	v_med3_f32 v6, v6, s28, v197
	v_mov_b32_e32 v5, 0
	v_cvt_pk_fp8_f32 v5, v8, v6
	v_mul_f32_e32 v7, v16, v40
	v_mul_f32_e32 v6, v17, v40
	v_med3_f32 v7, v7, s28, v197
	v_med3_f32 v6, v6, s28, v197
	v_cvt_pk_fp8_f32 v5, v7, v6 op_sel:[0,0,1]
	v_permlane32_swap_b32_e32 v2, v3
	s_nop 0
	v_permlane32_swap_b32_e32 v4, v5
	global_store_dwordx4 v[38:39], v[2:5], off offset:96
	s_barrier
	s_and_saveexec_b64 s[8:9], s[0:1]
	s_cbranch_execz .LBB0_353
	v_mov_b32_e32 v2, s2
	s_waitcnt vmcnt(4)
	ds_write_b32 v2, v198
	s_branch .LBB0_353

.LBB0_1015:
	v_mov_b32_e32 v222, 0
	s_and_saveexec_b64 s[18:19], s[0:1]
	s_cbranch_execz .LBB0_1019
	s_mov_b64 s[22:23], exec
	v_mbcnt_lo_u32_b32 v2, s22, 0
	v_mbcnt_hi_u32_b32 v2, s23, v2
	v_cmp_eq_u32_e32 vcc, 0, v2
	s_and_saveexec_b64 s[20:21], vcc
	s_cbranch_execz .LBB0_1018
	s_bcnt1_i32_b64 s22, s[22:23]
	v_mov_b32_e32 v3, s22
	v_readlane_b32 s22, v254, 46
	v_readlane_b32 s23, v254, 47
	s_nop 4
	global_atomic_add v222, v167, v3, s[22:23] sc0
.LBB0_1018:
	s_or_b64 exec, exec, s[20:21]
.LBB0_1019:
	s_or_b64 exec, exec, s[18:19]
	s_ashr_i32 s21, s87, 6
	s_lshl_b32 s18, s87, 8
	s_bfe_u32 s20, s87, 0x30003
	s_lshl_b32 s39, s21, 11
	s_and_b32 s18, s18, 0x700
	s_or_b32 s22, s39, s18
	s_mul_i32 s18, s20, 0x180
	s_add_u32 s18, s24, s18
	s_addc_u32 s19, s25, 0
	v_add_u32_e32 v190, s22, v199
	v_mov_b64_e32 v[2:3], s[18:19]
	v_mad_i64_i32 v[2:3], s[18:19], v190, s33, v[2:3]
	v_lshl_add_u64 v[14:15], v[2:3], 0, v[186:187]
	global_load_dwordx4 v[34:37], v[14:15], off offset:48
	global_load_dwordx4 v[38:41], v[14:15], off offset:32
	global_load_dwordx4 v[42:45], v[14:15], off offset:16
	global_load_dwordx4 v[46:49], v[14:15], off
	global_load_dwordx4 v[18:21], v[14:15], off offset:176
	global_load_dwordx4 v[22:25], v[14:15], off offset:160
	global_load_dwordx4 v[26:29], v[14:15], off offset:144
	global_load_dwordx4 v[30:33], v[14:15], off offset:128
	global_load_dwordx4 v[2:5], v[14:15], off offset:304
	global_load_dwordx4 v[10:13], v[14:15], off offset:288
	global_load_dwordx4 v[6:9], v[14:15], off offset:272
	s_nop 0
	global_load_dwordx4 v[14:17], v[14:15], off offset:256
	s_lshl_b32 s37, s20, 7
	s_add_u32 s18, s28, s37
	s_addc_u32 s19, s29, 0
	s_lshl_b32 s40, s21, 8
	s_add_i32 s38, s40, 0x8000
	s_and_saveexec_b64 s[20:21], s[6:7]
	s_cbranch_execz .LBB0_1021
	v_or_b32_e32 v50, s38, v213
	v_mov_b32_e32 v52, s19
	v_ashrrev_i32_e32 v51, 31, v50
	v_cndmask_b32_e64 v53, v171, v52, s[14:15]
	v_mov_b32_e32 v52, s18
	v_cndmask_b32_e64 v52, v170, v52, s[14:15]
	v_lshlrev_b64 v[50:51], v178, v[50:51]
	v_lshl_add_u64 v[50:51], v[52:53], 0, v[50:51]
	v_lshl_add_u64 v[50:51], v[50:51], 0, v[180:181]
	global_load_dwordx4 v[154:157], v[50:51], off

.LBB0_1053:
	ds_bpermute_b32 v68, v225, v226
	s_add_u32 s18, s26, s37
	v_lshlrev_b64 v[66:67], 11, v[190:191]
	s_addc_u32 s19, s27, 0
	v_lshl_add_u64 v[66:67], s[18:19], 0, v[66:67]
	s_waitcnt lgkmcnt(0)
	v_add_f32_e32 v68, v226, v68
	v_div_scale_f32 v69, s[20:21], v68, v68, 1.0
	v_rcp_f32_e32 v70, v69
	v_div_scale_f32 v71, vcc, 1.0, v68, 1.0
	v_lshl_add_u64 v[66:67], v[66:67], 0, v[176:177]
	v_fma_f32 v72, -v69, v70, 1.0
	v_fmac_f32_e32 v70, v72, v70
	v_mul_f32_e32 v72, v71, v70
	v_fma_f32 v73, -v69, v72, v71
	v_fmac_f32_e32 v72, v73, v70
	v_fma_f32 v69, -v69, v72, v71
	v_div_fmas_f32 v69, v69, v70, v72
	v_div_fixup_f32 v68, v69, v68, 1.0
	v_mul_f32_e32 v68, 0x41800000, v68
	v_mul_f32_e32 v50, v50, v68
	v_mul_f32_e32 v51, v51, v68
	v_med3_f32 v69, v50, s34, v220
	v_med3_f32 v51, v51, s34, v220
	v_mov_b32_e32 v50, 0
	v_cvt_pk_fp8_f32 v50, v69, v51
	v_mul_f32_e32 v52, v52, v68
	v_mul_f32_e32 v51, v53, v68
	v_med3_f32 v52, v52, s34, v220
	v_med3_f32 v51, v51, s34, v220
	v_cvt_pk_fp8_f32 v50, v52, v51 op_sel:[0,0,1]
	v_mul_f32_e32 v51, v54, v68
	v_mul_f32_e32 v52, v55, v68
	v_med3_f32 v51, v51, s34, v220
	v_med3_f32 v54, v52, s34, v220
	v_mov_b32_e32 v52, 0
	v_cvt_pk_fp8_f32 v52, v51, v54
	v_mul_f32_e32 v53, v56, v68
	v_mul_f32_e32 v51, v57, v68
	v_med3_f32 v53, v53, s34, v220
	v_med3_f32 v51, v51, s34, v220
	v_cvt_pk_fp8_f32 v52, v53, v51 op_sel:[0,0,1]
	v_mul_f32_e32 v51, v58, v68
	v_mul_f32_e32 v53, v59, v68
	v_med3_f32 v55, v51, s34, v220
	v_med3_f32 v53, v53, s34, v220
	v_mov_b32_e32 v51, 0
	v_cvt_pk_fp8_f32 v51, v55, v53
	v_mul_f32_e32 v54, v60, v68
	v_mul_f32_e32 v53, v61, v68
	v_med3_f32 v54, v54, s34, v220
	v_med3_f32 v53, v53, s34, v220
	v_cvt_pk_fp8_f32 v51, v54, v53 op_sel:[0,0,1]
	v_mul_f32_e32 v53, v62, v68
	v_mul_f32_e32 v54, v63, v68
	v_med3_f32 v56, v53, s34, v220
	v_med3_f32 v54, v54, s34, v220
	v_mov_b32_e32 v53, 0
	v_cvt_pk_fp8_f32 v53, v56, v54
	v_mul_f32_e32 v55, v64, v68
	v_mul_f32_e32 v54, v65, v68
	v_med3_f32 v55, v55, s34, v220
	v_med3_f32 v54, v54, s34, v220
	v_cvt_pk_fp8_f32 v53, v55, v54 op_sel:[0,0,1]
	v_permlane32_swap_b32_e32 v50, v51
	v_mul_f32_e32 v34, v34, v68
	v_permlane32_swap_b32_e32 v52, v53
	v_mul_f32_e32 v35, v35, v68
	global_store_dwordx4 v[66:67], v[50:53], off
	v_med3_f32 v35, v35, s34, v220
	v_mul_f32_e32 v36, v36, v68
	v_med3_f32 v50, v34, s34, v220
	v_mov_b32_e32 v34, 0
	v_cvt_pk_fp8_f32 v34, v50, v35
	v_mul_f32_e32 v35, v37, v68
	v_med3_f32 v36, v36, s34, v220
	v_med3_f32 v35, v35, s34, v220
	v_cvt_pk_fp8_f32 v34, v36, v35 op_sel:[0,0,1]
	v_mul_f32_e32 v35, v38, v68
	v_mul_f32_e32 v36, v39, v68
	v_med3_f32 v35, v35, s34, v220
	v_med3_f32 v38, v36, s34, v220
	v_mov_b32_e32 v36, 0
	v_cvt_pk_fp8_f32 v36, v35, v38
	v_mul_f32_e32 v37, v40, v68
	v_mul_f32_e32 v35, v41, v68
	v_med3_f32 v37, v37, s34, v220
	v_med3_f32 v35, v35, s34, v220
	v_cvt_pk_fp8_f32 v36, v37, v35 op_sel:[0,0,1]
	v_mul_f32_e32 v35, v42, v68
	v_mul_f32_e32 v37, v43, v68
	v_med3_f32 v39, v35, s34, v220
	v_med3_f32 v37, v37, s34, v220
	v_mov_b32_e32 v35, 0
	v_cvt_pk_fp8_f32 v35, v39, v37
	v_mul_f32_e32 v38, v44, v68
	v_mul_f32_e32 v37, v45, v68
	v_med3_f32 v38, v38, s34, v220
	v_med3_f32 v37, v37, s34, v220
	v_cvt_pk_fp8_f32 v35, v38, v37 op_sel:[0,0,1]
	v_mul_f32_e32 v37, v46, v68
	v_mul_f32_e32 v38, v47, v68
	v_med3_f32 v40, v37, s34, v220
	v_med3_f32 v38, v38, s34, v220
	v_mov_b32_e32 v37, 0
	v_cvt_pk_fp8_f32 v37, v40, v38
	v_mul_f32_e32 v39, v48, v68
	v_mul_f32_e32 v38, v49, v68
	v_med3_f32 v39, v39, s34, v220
	v_med3_f32 v38, v38, s34, v220
	v_cvt_pk_fp8_f32 v37, v39, v38 op_sel:[0,0,1]
	v_permlane32_swap_b32_e32 v34, v35
	v_mul_f32_e32 v18, v18, v68
	v_permlane32_swap_b32_e32 v36, v37
	v_mul_f32_e32 v19, v19, v68
	global_store_dwordx4 v[66:67], v[34:37], off offset:32
	v_med3_f32 v19, v19, s34, v220
	v_mul_f32_e32 v20, v20, v68
	v_med3_f32 v34, v18, s34, v220
	v_mov_b32_e32 v18, 0
	v_cvt_pk_fp8_f32 v18, v34, v19
	v_mul_f32_e32 v19, v21, v68
	v_med3_f32 v20, v20, s34, v220
	v_med3_f32 v19, v19, s34, v220
	v_cvt_pk_fp8_f32 v18, v20, v19 op_sel:[0,0,1]
	v_mul_f32_e32 v19, v22, v68
	v_mul_f32_e32 v20, v23, v68
	v_med3_f32 v19, v19, s34, v220
	v_med3_f32 v22, v20, s34, v220
	v_mov_b32_e32 v20, 0
	v_cvt_pk_fp8_f32 v20, v19, v22
	v_mul_f32_e32 v21, v24, v68
	v_mul_f32_e32 v19, v25, v68
	v_med3_f32 v21, v21, s34, v220
	v_med3_f32 v19, v19, s34, v220
	v_cvt_pk_fp8_f32 v20, v21, v19 op_sel:[0,0,1]
	v_mul_f32_e32 v19, v26, v68
	v_mul_f32_e32 v21, v27, v68
	v_med3_f32 v23, v19, s34, v220
	v_med3_f32 v21, v21, s34, v220
	v_mov_b32_e32 v19, 0
	v_cvt_pk_fp8_f32 v19, v23, v21
	v_mul_f32_e32 v22, v28, v68
	v_mul_f32_e32 v21, v29, v68
	v_med3_f32 v22, v22, s34, v220
	v_med3_f32 v21, v21, s34, v220
	v_cvt_pk_fp8_f32 v19, v22, v21 op_sel:[0,0,1]
	v_mul_f32_e32 v21, v30, v68
	v_mul_f32_e32 v22, v31, v68
	v_med3_f32 v24, v21, s34, v220
	v_med3_f32 v22, v22, s34, v220
	v_mov_b32_e32 v21, 0
	v_cvt_pk_fp8_f32 v21, v24, v22
	v_mul_f32_e32 v23, v32, v68
	v_mul_f32_e32 v22, v33, v68
	v_med3_f32 v23, v23, s34, v220
	v_med3_f32 v22, v22, s34, v220
	v_cvt_pk_fp8_f32 v21, v23, v22 op_sel:[0,0,1]
	v_permlane32_swap_b32_e32 v18, v19
	v_mul_f32_e32 v2, v2, v68
	v_permlane32_swap_b32_e32 v20, v21
	v_mul_f32_e32 v3, v3, v68
	global_store_dwordx4 v[66:67], v[18:21], off offset:64
	v_med3_f32 v3, v3, s34, v220
	v_mul_f32_e32 v4, v4, v68
	v_med3_f32 v18, v2, s34, v220
	v_mov_b32_e32 v2, 0
	v_cvt_pk_fp8_f32 v2, v18, v3
	v_mul_f32_e32 v3, v5, v68
	v_med3_f32 v4, v4, s34, v220
	v_med3_f32 v3, v3, s34, v220
	v_cvt_pk_fp8_f32 v2, v4, v3 op_sel:[0,0,1]
	v_mul_f32_e32 v3, v6, v68
	v_mul_f32_e32 v4, v7, v68
	v_med3_f32 v3, v3, s34, v220
	v_med3_f32 v6, v4, s34, v220
	v_mov_b32_e32 v4, 0
	v_cvt_pk_fp8_f32 v4, v3, v6
	v_mul_f32_e32 v5, v8, v68
	v_mul_f32_e32 v3, v9, v68
	v_med3_f32 v5, v5, s34, v220
	v_med3_f32 v3, v3, s34, v220
	v_cvt_pk_fp8_f32 v4, v5, v3 op_sel:[0,0,1]
	v_mul_f32_e32 v3, v10, v68
	v_mul_f32_e32 v5, v11, v68
	v_med3_f32 v7, v3, s34, v220
	v_med3_f32 v5, v5, s34, v220
	v_mov_b32_e32 v3, 0
	v_cvt_pk_fp8_f32 v3, v7, v5
	v_mul_f32_e32 v6, v12, v68
	v_mul_f32_e32 v5, v13, v68
	v_med3_f32 v6, v6, s34, v220
	v_med3_f32 v5, v5, s34, v220
	v_cvt_pk_fp8_f32 v3, v6, v5 op_sel:[0,0,1]
	v_mul_f32_e32 v5, v14, v68
	v_mul_f32_e32 v6, v15, v68
	v_med3_f32 v8, v5, s34, v220
	v_med3_f32 v6, v6, s34, v220
	v_mov_b32_e32 v5, 0
	v_cvt_pk_fp8_f32 v5, v8, v6
	v_mul_f32_e32 v7, v16, v68
	v_mul_f32_e32 v6, v17, v68
	v_med3_f32 v7, v7, s34, v220
	v_med3_f32 v6, v6, s34, v220
	v_cvt_pk_fp8_f32 v5, v7, v6 op_sel:[0,0,1]
	v_permlane32_swap_b32_e32 v2, v3
	s_nop 0
	v_permlane32_swap_b32_e32 v4, v5
	global_store_dwordx4 v[66:67], v[2:5], off offset:96
	s_barrier
	s_and_saveexec_b64 s[18:19], s[0:1]
	s_cbranch_execz .LBB0_1014
	v_mov_b32_e32 v2, s2
	s_waitcnt vmcnt(4)
	ds_write_b32 v2, v222
	s_branch .LBB0_1014

.LBB0_1058:
	v_mov_b32_e32 v224, 0
	s_and_saveexec_b64 s[88:89], s[0:1]
	s_cbranch_execz .LBB0_1062
	s_mov_b64 s[84:85], exec
	v_mbcnt_lo_u32_b32 v3, s84, 0
	v_mbcnt_hi_u32_b32 v3, s85, v3
	v_cmp_eq_u32_e32 vcc, 0, v3
	s_and_saveexec_b64 s[94:95], vcc
	s_cbranch_execz .LBB0_1061
	s_bcnt1_i32_b64 s3, s[84:85]
	v_readlane_b32 s4, v254, 46
	v_mov_b32_e32 v4, s3
	v_readlane_b32 s5, v254, 47
	s_nop 4
	global_atomic_add v224, v2, v4, s[4:5] sc0
.LBB0_1061:
	s_or_b64 exec, exec, s[94:95]
.LBB0_1062:
	s_or_b64 exec, exec, s[88:89]
	s_bfe_u32 s3, s87, 0x30003
	s_mov_b64 s[88:89], exec
	v_readlane_b32 s4, v254, 57
	v_readlane_b32 s5, v254, 58
	s_and_b64 s[4:5], s[88:89], s[4:5]
	s_mov_b64 exec, s[4:5]
	s_cbranch_execz .LBB0_1064
	v_readlane_b32 s4, v254, 61
	v_readlane_b32 s5, v254, 62
	s_mov_b32 s9, s5
	s_mul_i32 s8, s3, 0x744
	v_lshl_add_u64 v[4:5], v[190:191], 0, s[8:9]
	global_load_dword v3, v[4:5], off
	v_writelane_b32 v254, s4, 61
	s_waitcnt vmcnt(0)
	ds_write_b32 v216, v3 offset:18432
	v_writelane_b32 v254, s5, 62

.LBB0_1160:
	v_cmp_lt_i32_e32 vcc, v225, v227
	v_readlane_b32 s3, v254, 36
	v_ashrrev_i32_e32 v199, 31, v198
	v_cndmask_b32_e32 v3, v226, v225, vcc
	v_lshlrev_b32_e32 v3, 2, v3
	ds_bpermute_b32 v3, v3, v228
	s_add_u32 s4, s3, s90
	v_readlane_b32 s3, v254, 37
	s_addc_u32 s5, s3, 0
	s_waitcnt lgkmcnt(0)
	v_add_f32_e32 v3, v228, v3
	v_div_scale_f32 v68, s[8:9], v3, v3, 1.0
	v_rcp_f32_e32 v69, v68
	v_div_scale_f32 v70, vcc, 1.0, v3, 1.0
	v_fma_f32 v71, -v68, v69, 1.0
	v_fmac_f32_e32 v69, v71, v69
	v_mul_f32_e32 v71, v70, v69
	v_fma_f32 v72, -v68, v71, v70
	v_fmac_f32_e32 v71, v72, v69
	v_fma_f32 v68, -v68, v71, v70
	v_div_fmas_f32 v68, v68, v69, v71
	v_div_fixup_f32 v3, v68, v3, 1.0
	v_mul_f32_e32 v3, 0x41800000, v3
	v_mul_f32_e32 v52, v52, v3
	v_mul_f32_e32 v53, v53, v3
	v_med3_f32 v70, v52, s33, v223
	v_med3_f32 v53, v53, s33, v223
	v_mov_b32_e32 v52, 0
	v_cvt_pk_fp8_f32 v52, v70, v53
	v_mul_f32_e32 v54, v54, v3
	v_mul_f32_e32 v53, v55, v3
	v_med3_f32 v54, v54, s33, v223
	v_med3_f32 v53, v53, s33, v223
	v_cvt_pk_fp8_f32 v52, v54, v53 op_sel:[0,0,1]
	v_mul_f32_e32 v53, v56, v3
	v_mul_f32_e32 v54, v57, v3
	v_med3_f32 v53, v53, s33, v223
	v_med3_f32 v56, v54, s33, v223
	v_mov_b32_e32 v54, 0
	v_cvt_pk_fp8_f32 v54, v53, v56
	v_mul_f32_e32 v55, v58, v3
	v_mul_f32_e32 v53, v59, v3
	v_med3_f32 v55, v55, s33, v223
	v_med3_f32 v53, v53, s33, v223
	v_cvt_pk_fp8_f32 v54, v55, v53 op_sel:[0,0,1]
	v_mul_f32_e32 v53, v60, v3
	v_mul_f32_e32 v55, v61, v3
	v_med3_f32 v57, v53, s33, v223
	v_med3_f32 v55, v55, s33, v223
	v_mov_b32_e32 v53, 0
	v_cvt_pk_fp8_f32 v53, v57, v55
	v_mul_f32_e32 v56, v62, v3
	v_mul_f32_e32 v55, v63, v3
	v_med3_f32 v56, v56, s33, v223
	v_med3_f32 v55, v55, s33, v223
	v_cvt_pk_fp8_f32 v53, v56, v55 op_sel:[0,0,1]
	v_mul_f32_e32 v55, v64, v3
	v_mul_f32_e32 v56, v65, v3
	v_med3_f32 v58, v55, s33, v223
	v_med3_f32 v56, v56, s33, v223
	v_mov_b32_e32 v55, 0
	v_cvt_pk_fp8_f32 v55, v58, v56
	v_mul_f32_e32 v57, v66, v3
	v_mul_f32_e32 v56, v67, v3
	v_med3_f32 v57, v57, s33, v223
	v_med3_f32 v56, v56, s33, v223
	v_cvt_pk_fp8_f32 v55, v57, v56 op_sel:[0,0,1]
	v_lshlrev_b64 v[68:69], 11, v[198:199]
	v_lshl_add_u64 v[68:69], s[4:5], 0, v[68:69]
	v_lshl_add_u64 v[68:69], v[68:69], 0, v[194:195]
	v_permlane32_swap_b32_e32 v52, v53
	v_permlane32_swap_b32_e32 v54, v55
	v_mul_f32_e32 v36, v36, v3
	v_mul_f32_e32 v37, v37, v3
	global_store_dwordx4 v[68:69], v[52:55], off
	v_med3_f32 v37, v37, s33, v223
	v_mul_f32_e32 v38, v38, v3
	v_med3_f32 v52, v36, s33, v223
	v_mov_b32_e32 v36, 0
	v_cvt_pk_fp8_f32 v36, v52, v37
	v_mul_f32_e32 v37, v39, v3
	v_med3_f32 v38, v38, s33, v223
	v_med3_f32 v37, v37, s33, v223
	v_cvt_pk_fp8_f32 v36, v38, v37 op_sel:[0,0,1]
	v_mul_f32_e32 v37, v40, v3
	v_mul_f32_e32 v38, v41, v3
	v_med3_f32 v37, v37, s33, v223
	v_med3_f32 v40, v38, s33, v223
	v_mov_b32_e32 v38, 0
	v_cvt_pk_fp8_f32 v38, v37, v40
	v_mul_f32_e32 v39, v42, v3
	v_mul_f32_e32 v37, v43, v3
	v_med3_f32 v39, v39, s33, v223
	v_med3_f32 v37, v37, s33, v223
	v_cvt_pk_fp8_f32 v38, v39, v37 op_sel:[0,0,1]
	v_mul_f32_e32 v37, v44, v3
	v_mul_f32_e32 v39, v45, v3
	v_med3_f32 v41, v37, s33, v223
	v_med3_f32 v39, v39, s33, v223
	v_mov_b32_e32 v37, 0
	v_cvt_pk_fp8_f32 v37, v41, v39
	v_mul_f32_e32 v40, v46, v3
	v_mul_f32_e32 v39, v47, v3
	v_med3_f32 v40, v40, s33, v223
	v_med3_f32 v39, v39, s33, v223
	v_cvt_pk_fp8_f32 v37, v40, v39 op_sel:[0,0,1]
	v_mul_f32_e32 v39, v48, v3
	v_mul_f32_e32 v40, v49, v3
	v_med3_f32 v42, v39, s33, v223
	v_med3_f32 v40, v40, s33, v223
	v_mov_b32_e32 v39, 0
	v_cvt_pk_fp8_f32 v39, v42, v40
	v_mul_f32_e32 v41, v50, v3
	v_mul_f32_e32 v40, v51, v3
	v_med3_f32 v41, v41, s33, v223
	v_med3_f32 v40, v40, s33, v223
	v_cvt_pk_fp8_f32 v39, v41, v40 op_sel:[0,0,1]
	v_permlane32_swap_b32_e32 v36, v37
	v_mul_f32_e32 v20, v20, v3
	v_permlane32_swap_b32_e32 v38, v39
	v_mul_f32_e32 v21, v21, v3
	global_store_dwordx4 v[68:69], v[36:39], off offset:32
	v_med3_f32 v21, v21, s33, v223
	v_mul_f32_e32 v22, v22, v3
	v_med3_f32 v36, v20, s33, v223
	v_mov_b32_e32 v20, 0
	v_cvt_pk_fp8_f32 v20, v36, v21
	v_mul_f32_e32 v21, v23, v3
	v_med3_f32 v22, v22, s33, v223
	v_med3_f32 v21, v21, s33, v223
	v_cvt_pk_fp8_f32 v20, v22, v21 op_sel:[0,0,1]
	v_mul_f32_e32 v21, v24, v3
	v_mul_f32_e32 v22, v25, v3
	v_med3_f32 v21, v21, s33, v223
	v_med3_f32 v24, v22, s33, v223
	v_mov_b32_e32 v22, 0
	v_cvt_pk_fp8_f32 v22, v21, v24
	v_mul_f32_e32 v23, v26, v3
	v_mul_f32_e32 v21, v27, v3
	v_med3_f32 v23, v23, s33, v223
	v_med3_f32 v21, v21, s33, v223
	v_cvt_pk_fp8_f32 v22, v23, v21 op_sel:[0,0,1]
	v_mul_f32_e32 v21, v28, v3
	v_mul_f32_e32 v23, v29, v3
	v_med3_f32 v25, v21, s33, v223
	v_med3_f32 v23, v23, s33, v223
	v_mov_b32_e32 v21, 0
	v_cvt_pk_fp8_f32 v21, v25, v23
	v_mul_f32_e32 v24, v30, v3
	v_mul_f32_e32 v23, v31, v3
	v_med3_f32 v24, v24, s33, v223
	v_med3_f32 v23, v23, s33, v223
	v_cvt_pk_fp8_f32 v21, v24, v23 op_sel:[0,0,1]
	v_mul_f32_e32 v23, v32, v3
	v_mul_f32_e32 v24, v33, v3
	v_med3_f32 v26, v23, s33, v223
	v_med3_f32 v24, v24, s33, v223
	v_mov_b32_e32 v23, 0
	v_cvt_pk_fp8_f32 v23, v26, v24
	v_mul_f32_e32 v25, v34, v3
	v_mul_f32_e32 v24, v35, v3
	v_med3_f32 v25, v25, s33, v223
	v_med3_f32 v24, v24, s33, v223
	v_cvt_pk_fp8_f32 v23, v25, v24 op_sel:[0,0,1]
	v_permlane32_swap_b32_e32 v20, v21
	v_mul_f32_e32 v4, v4, v3
	v_permlane32_swap_b32_e32 v22, v23
	v_mul_f32_e32 v5, v5, v3
	global_store_dwordx4 v[68:69], v[20:23], off offset:64
	v_med3_f32 v5, v5, s33, v223
	v_mul_f32_e32 v6, v6, v3
	v_med3_f32 v20, v4, s33, v223
	v_mov_b32_e32 v4, 0
	v_cvt_pk_fp8_f32 v4, v20, v5
	v_mul_f32_e32 v5, v7, v3
	v_med3_f32 v6, v6, s33, v223
	v_med3_f32 v5, v5, s33, v223
	v_cvt_pk_fp8_f32 v4, v6, v5 op_sel:[0,0,1]
	v_mul_f32_e32 v5, v8, v3
	v_mul_f32_e32 v6, v9, v3
	v_med3_f32 v5, v5, s33, v223
	v_med3_f32 v8, v6, s33, v223
	v_mov_b32_e32 v6, 0
	v_cvt_pk_fp8_f32 v6, v5, v8
	v_mul_f32_e32 v7, v10, v3
	v_mul_f32_e32 v5, v11, v3
	v_med3_f32 v7, v7, s33, v223
	v_med3_f32 v5, v5, s33, v223
	v_cvt_pk_fp8_f32 v6, v7, v5 op_sel:[0,0,1]
	v_mul_f32_e32 v5, v12, v3
	v_mul_f32_e32 v7, v13, v3
	v_med3_f32 v9, v5, s33, v223
	v_med3_f32 v7, v7, s33, v223
	v_mov_b32_e32 v5, 0
	v_cvt_pk_fp8_f32 v5, v9, v7
	v_mul_f32_e32 v8, v14, v3
	v_mul_f32_e32 v7, v15, v3
	v_med3_f32 v8, v8, s33, v223
	v_med3_f32 v7, v7, s33, v223
	v_cvt_pk_fp8_f32 v5, v8, v7 op_sel:[0,0,1]
	v_mul_f32_e32 v7, v16, v3
	v_mul_f32_e32 v8, v17, v3
	v_med3_f32 v10, v7, s33, v223
	v_med3_f32 v8, v8, s33, v223
	v_mov_b32_e32 v7, 0
	v_cvt_pk_fp8_f32 v7, v10, v8
	v_mul_f32_e32 v9, v18, v3
	v_mul_f32_e32 v3, v19, v3
	v_med3_f32 v8, v9, s33, v223
	v_med3_f32 v3, v3, s33, v223
	v_cvt_pk_fp8_f32 v7, v8, v3 op_sel:[0,0,1]
	v_permlane32_swap_b32_e32 v4, v5
	s_nop 0
	v_permlane32_swap_b32_e32 v6, v7
	global_store_dwordx4 v[68:69], v[4:7], off offset:96
	s_barrier
	s_and_saveexec_b64 s[84:85], s[0:1]
	s_cbranch_execz .LBB0_1057
	v_readlane_b32 s3, v255, 1
	s_nop 1
	v_mov_b32_e32 v3, s3
	s_waitcnt vmcnt(4)
	ds_write_b32 v3, v224
	s_branch .LBB0_1057
